# cache policy: nt on k_localsort read-once HBM edge loads
# speedup vs baseline: 1.0551x; 1.0435x over previous
_Z11k_localsortPKiS0_S0_PjPtPiPKjPKfS7_S7_S7_S7_S7_S7_S7_S7_S7_PDF16_S8_S8_PfS9_:
	s_cmpk_lt_u32 s2, 0xde
	s_mov_b64 s[4:5], -1
	s_cbranch_scc0 .LBB1_84
	s_load_dwordx4 s[4:7], s[0:1], 0x0
	s_load_dwordx2 s[8:9], s[0:1], 0x10
	s_movk_i32 s3, 0x187
	v_cmp_gt_u32_e64 s[50:51], s3, v0
	v_lshlrev_b32_e32 v38, 2, v0
	s_and_saveexec_b64 s[10:11], s[50:51]
	v_mov_b32_e32 v1, 0
	ds_write_b32 v38, v1
	s_or_b64 exec, exec, s[10:11]
	s_mul_i32 s3, s2, 0x6f
	s_bfe_u32 s64, s3, 0x3000d
	v_mov_b32_e32 v1, 0x4a
	s_mul_i32 s3, s64, 0xffffffb6
	v_sub_co_u32_e32 v1, vcc, s2, v1
	s_add_i32 s3, s3, s2
	v_readfirstlane_b32 s10, v1
	s_cmpk_lt_u32 s10, 0x4a
	s_waitcnt lgkmcnt(0)
	s_cselect_b32 s8, s6, s8
	s_cselect_b32 s9, s7, s9
	s_and_b64 s[6:7], vcc, exec
	s_cselect_b32 s9, s5, s9
	s_cselect_b32 s8, s4, s8
	s_lshl_b32 s4, s3, 14
	s_ashr_i32 s5, s4, 31
	s_lshl_b64 s[6:7], s[4:5], 2
	s_add_u32 s6, s8, s6
	s_addc_u32 s7, s9, s7
	s_add_u32 s8, s6, 0x493e00
	s_addc_u32 s9, s7, 0
	s_sub_i32 s3, 0x124f80, s4
	s_min_i32 s3, s3, 0x4000
	s_ashr_i32 s33, s3, 2
	v_cmp_gt_i32_e32 vcc, s33, v0
	v_mov_b32_e32 v10, -1
	v_mov_b32_e32 v14, 0
	v_lshlrev_b32_e32 v34, 4, v0
	v_mov_b32_e32 v26, 0
	v_mov_b32_e32 v27, 0
	v_mov_b32_e32 v28, 0
	v_mov_b32_e32 v29, 0
	v_mov_b32_e32 v30, -1
	v_mov_b32_e32 v31, -1
	v_mov_b32_e32 v32, -1
	v_mov_b32_e32 v33, -1
	s_and_saveexec_b64 s[4:5], vcc
	s_cbranch_execz .LBB1_5
	global_load_dwordx4 v[30:33], v34, s[8:9] nt
	global_load_dwordx4 v[26:29], v34, s[6:7] nt
.LBB1_5:
	s_or_b64 exec, exec, s[4:5]
	v_or_b32_e32 v1, 0x400, v0
	v_cmp_gt_i32_e64 s[4:5], s33, v1
	v_mov_b32_e32 v15, 0
	v_mov_b32_e32 v16, 0
	v_mov_b32_e32 v17, 0
	v_mov_b32_e32 v11, -1
	v_mov_b32_e32 v12, -1
	v_mov_b32_e32 v13, -1
	s_and_saveexec_b64 s[10:11], s[4:5]
	s_cbranch_execz .LBB1_7
	v_lshlrev_b32_e32 v1, 4, v1
	global_load_dwordx4 v[10:13], v1, s[8:9] nt
	global_load_dwordx4 v[14:17], v1, s[6:7] nt
.LBB1_7:
	s_or_b64 exec, exec, s[10:11]
	v_or_b32_e32 v1, 0x800, v0
	v_cmp_gt_i32_e64 s[4:5], s33, v1
	v_mov_b32_e32 v2, -1
	v_mov_b32_e32 v6, 0
	v_mov_b32_e32 v18, 0
	v_mov_b32_e32 v19, 0
	v_mov_b32_e32 v20, 0
	v_mov_b32_e32 v21, 0
	v_mov_b32_e32 v22, -1
	v_mov_b32_e32 v23, -1
	v_mov_b32_e32 v24, -1
	v_mov_b32_e32 v25, -1
	s_and_saveexec_b64 s[10:11], s[4:5]
	s_cbranch_execz .LBB1_9
	v_lshlrev_b32_e32 v1, 4, v1
	global_load_dwordx4 v[22:25], v1, s[8:9] nt
	global_load_dwordx4 v[18:21], v1, s[6:7] nt
.LBB1_9:
	s_or_b64 exec, exec, s[10:11]
	s_load_dwordx8 s[56:63], s[0:1], 0x18
	v_or_b32_e32 v1, 0xc00, v0
	v_cmp_gt_i32_e64 s[4:5], s33, v1
	v_mov_b32_e32 v7, 0
	v_mov_b32_e32 v8, 0
	v_mov_b32_e32 v9, 0
	v_mov_b32_e32 v3, -1
	v_mov_b32_e32 v4, -1
	v_mov_b32_e32 v5, -1
	s_and_saveexec_b64 s[10:11], s[4:5]
	s_cbranch_execz .LBB1_11
	v_lshlrev_b32_e32 v1, 4, v1
	global_load_dwordx4 v[2:5], v1, s[8:9] nt
	global_load_dwordx4 v[6:9], v1, s[6:7] nt
